# v14 + P0a: the w_out / w_query column-maxima loads (read once in this phase) marked nt like the w_in ones
# speedup vs baseline: 1.0078x; 1.0053x over previous
; DI void p0_colmaxq_item(Frame& F, int item) {
;     const int lane = F.lane, nblk = D / 32, kb = item / nblk, nb = item % nblk, k0 = 64 * kb, n0 = 32 * nb;
;     float m = 0.f;
; #pragma unroll 8
;     for (int i = 0; i < 32; ++i) { const int kk = 2 * i + (lane >> 5); m = fmaxf(m, fabsf(F.wq[(size_t)(k0 + kk) * D + n0 + (lane & 31)])); }
;     m = fmaxf(m, __shfl_xor(m, 32));
;     if (lane < 32) F.CMAXQ[(size_t)kb * D + n0 + lane] = m;
; }
.LBB0_22:
	s_lshl_b32 s0, s44, 2
	s_lshl_b32 s2, s33, 5
	s_and_b32 s47, s33, 0x7c0
	s_and_b32 s48, s0, 0x1f80
	s_mov_b32 s0, s2
	v_writelane_b32 v252, s0, 53
	s_and_b32 s49, s2, 0x7e0
	v_or_b32_e32 v25, s47, v46
	v_writelane_b32 v252, s1, 54
	s_cmpk_gt_u32 s33, 0x1fff
	s_mov_b64 s[0:1], -1
	s_waitcnt lgkmcnt(0)
	v_add_u32_e32 v12, 4, v25
	v_add_u32_e32 v14, 8, v25
	v_add_u32_e32 v16, 12, v25
	v_add_u32_e32 v18, 16, v25
	v_add_u32_e32 v20, 20, v25
	v_add_u32_e32 v22, 24, v25
	v_add_u32_e32 v24, 28, v25
	s_cbranch_scc0 .LBB0_78
	v_readfirstlane_b32 s2, v4
	v_readfirstlane_b32 s3, v5
	s_lshl_b32 s0, s49, 2
	s_lshl_b32 s4, s47, 13
	s_add_i32 s0, s0, s4
	s_add_u32 s0, s2, s0
	s_addc_u32 s1, s3, 0
	v_and_b32_e32 v1, 31, v148
	v_lshlrev_b32_e32 v1, 2, v1
	v_lshl_or_b32 v2, v46, 13, v1
	global_load_dword v12, v2, s[0:1] nt
	s_add_u32 s0, s0, 0x4000
	s_addc_u32 s1, s1, 0
	global_load_dword v13, v2, s[0:1] nt
	s_add_u32 s0, s0, 0x4000
	s_addc_u32 s1, s1, 0
	global_load_dword v14, v2, s[0:1] nt
	s_add_u32 s0, s0, 0x4000
	s_addc_u32 s1, s1, 0
	global_load_dword v15, v2, s[0:1] nt
	s_add_u32 s0, s0, 0x4000
	s_addc_u32 s1, s1, 0
	global_load_dword v16, v2, s[0:1] nt
	s_add_u32 s0, s0, 0x4000
	s_addc_u32 s1, s1, 0
	global_load_dword v17, v2, s[0:1] nt
	s_add_u32 s0, s0, 0x4000
	s_addc_u32 s1, s1, 0
	global_load_dword v18, v2, s[0:1] nt
	s_add_u32 s0, s0, 0x4000
	s_addc_u32 s1, s1, 0
	global_load_dword v19, v2, s[0:1] nt
	s_add_u32 s0, s0, 0x4000
	s_addc_u32 s1, s1, 0
	global_load_dword v20, v2, s[0:1] nt
	s_add_u32 s0, s0, 0x4000
	s_addc_u32 s1, s1, 0
	global_load_dword v21, v2, s[0:1] nt
	s_add_u32 s0, s0, 0x4000
	s_addc_u32 s1, s1, 0
	global_load_dword v22, v2, s[0:1] nt
	s_add_u32 s0, s0, 0x4000
	s_addc_u32 s1, s1, 0
	global_load_dword v23, v2, s[0:1] nt
	s_add_u32 s0, s0, 0x4000
	s_addc_u32 s1, s1, 0
	global_load_dword v24, v2, s[0:1] nt
	s_add_u32 s0, s0, 0x4000
	s_addc_u32 s1, s1, 0
	global_load_dword v25, v2, s[0:1] nt
	s_add_u32 s0, s0, 0x4000
	s_addc_u32 s1, s1, 0
	global_load_dword v26, v2, s[0:1] nt
	s_add_u32 s0, s0, 0x4000
	s_addc_u32 s1, s1, 0
	global_load_dword v27, v2, s[0:1] nt
	s_add_u32 s0, s0, 0x4000
	s_addc_u32 s1, s1, 0
	global_load_dword v28, v2, s[0:1] nt
	s_add_u32 s0, s0, 0x4000
	s_addc_u32 s1, s1, 0
	global_load_dword v29, v2, s[0:1] nt
	s_add_u32 s0, s0, 0x4000
	s_addc_u32 s1, s1, 0
	global_load_dword v30, v2, s[0:1] nt
	s_add_u32 s0, s0, 0x4000
	s_addc_u32 s1, s1, 0
	global_load_dword v31, v2, s[0:1] nt
	s_add_u32 s0, s0, 0x4000
	s_addc_u32 s1, s1, 0
	global_load_dword v32, v2, s[0:1] nt
	s_add_u32 s0, s0, 0x4000
	s_addc_u32 s1, s1, 0
	global_load_dword v33, v2, s[0:1] nt
	s_add_u32 s0, s0, 0x4000
	s_addc_u32 s1, s1, 0
	global_load_dword v34, v2, s[0:1] nt
	s_add_u32 s0, s0, 0x4000
	s_addc_u32 s1, s1, 0
	global_load_dword v35, v2, s[0:1] nt
	s_add_u32 s0, s0, 0x4000
	s_addc_u32 s1, s1, 0
	global_load_dword v36, v2, s[0:1] nt
	s_add_u32 s0, s0, 0x4000
	s_addc_u32 s1, s1, 0
	global_load_dword v37, v2, s[0:1] nt
	s_add_u32 s0, s0, 0x4000
	s_addc_u32 s1, s1, 0
	global_load_dword v38, v2, s[0:1] nt
	s_add_u32 s0, s0, 0x4000
	s_addc_u32 s1, s1, 0
	global_load_dword v39, v2, s[0:1] nt
	s_add_u32 s0, s0, 0x4000
	s_addc_u32 s1, s1, 0
	global_load_dword v40, v2, s[0:1] nt
	s_add_u32 s0, s0, 0x4000
	s_addc_u32 s1, s1, 0
	global_load_dword v41, v2, s[0:1] nt
	s_add_u32 s0, s0, 0x4000
	s_addc_u32 s1, s1, 0
	global_load_dword v42, v2, s[0:1] nt
	s_add_u32 s0, s0, 0x4000
	s_addc_u32 s1, s1, 0
	global_load_dword v43, v2, s[0:1] nt
	s_waitcnt vmcnt(29)
	v_max3_f32 v1, |v12|, |v13|, |v14|
	s_waitcnt vmcnt(27)
	v_max3_f32 v1, v1, |v15|, |v16|
	s_waitcnt vmcnt(25)
	v_max3_f32 v1, v1, |v17|, |v18|
	s_waitcnt vmcnt(23)
	v_max3_f32 v1, v1, |v19|, |v20|
	s_waitcnt vmcnt(21)
	v_max3_f32 v1, v1, |v21|, |v22|
	s_waitcnt vmcnt(19)
	v_max3_f32 v1, v1, |v23|, |v24|
	s_waitcnt vmcnt(17)
	v_max3_f32 v1, v1, |v25|, |v26|
	s_waitcnt vmcnt(15)
	v_max3_f32 v1, v1, |v27|, |v28|
	s_waitcnt vmcnt(13)
	v_max3_f32 v1, v1, |v29|, |v30|
	s_waitcnt vmcnt(11)
	v_max3_f32 v1, v1, |v31|, |v32|
	s_waitcnt vmcnt(9)
	v_max3_f32 v1, v1, |v33|, |v34|
	s_waitcnt vmcnt(7)
	v_max3_f32 v1, v1, |v35|, |v36|
	s_waitcnt vmcnt(5)
	v_max3_f32 v1, v1, |v37|, |v38|
	s_waitcnt vmcnt(3)
	v_max3_f32 v1, v1, |v39|, |v40|
	s_waitcnt vmcnt(1)
	v_max3_f32 v1, v1, |v41|, |v42|
	s_waitcnt vmcnt(0)
	v_max_f32_e64 v1, v1, |v43|
	v_xor_b32_e32 v2, 32, v54
	v_lshlrev_b32_e32 v2, 2, v2
	ds_bpermute_b32 v2, v2, v1
	v_readlane_b32 s2, v252, 39
	v_readlane_b32 s3, v252, 40
	s_lshl_b32 s4, s33, 7
	s_sub_u32 s4, s4, 0x100000
	s_add_u32 s2, s2, s4
	s_addc_u32 s3, s3, 0
	v_readlane_b32 s22, v252, 51
	v_readlane_b32 s23, v252, 52
	s_waitcnt lgkmcnt(0)
	v_max_f32_e32 v1, v1, v2
	v_lshlrev_b32_e32 v2, 2, v148
	s_and_saveexec_b64 s[4:5], s[22:23]
	global_store_dword v2, v1, s[2:3]
	s_or_b64 exec, exec, s[4:5]
	s_mov_b64 s[0:1], 0
; DI void p0_colmaxo_item(Frame& F, int item) {
;     const int lane = F.lane, nblk = D / 32, kb = item / nblk, nb = item % nblk, k0 = 64 * kb, n0 = 32 * nb;
;     float m = 0.f;
; #pragma unroll 8
;     for (int i = 0; i < 32; ++i) { const int kk = 2 * i + (lane >> 5); m = fmaxf(m, fabsf(F.w_out[(size_t)(k0 + kk) * D + n0 + (lane & 31)])); }
;     m = fmaxf(m, __shfl_xor(m, 32));
;     if (lane < 32) F.CMAXO[(size_t)kb * D + n0 + lane] = m;
; }
.LBB0_78:
	s_and_b64 vcc, exec, s[0:1]
	s_cbranch_vccz .LBB0_134
	s_waitcnt lgkmcnt(0)
	v_readfirstlane_b32 s2, v8
	v_readfirstlane_b32 s3, v9
	s_lshl_b32 s0, s49, 2
	s_lshl_b32 s4, s47, 13
	s_add_i32 s0, s0, s4
	s_add_u32 s0, s2, s0
	s_addc_u32 s1, s3, 0
	v_and_b32_e32 v1, 31, v148
	v_lshlrev_b32_e32 v1, 2, v1
	v_lshl_or_b32 v2, v46, 13, v1
	global_load_dword v12, v2, s[0:1] nt
	s_add_u32 s0, s0, 0x4000
	s_addc_u32 s1, s1, 0
	global_load_dword v13, v2, s[0:1] nt
	s_add_u32 s0, s0, 0x4000
	s_addc_u32 s1, s1, 0
	global_load_dword v14, v2, s[0:1] nt
	s_add_u32 s0, s0, 0x4000
	s_addc_u32 s1, s1, 0
	global_load_dword v15, v2, s[0:1] nt
	s_add_u32 s0, s0, 0x4000
	s_addc_u32 s1, s1, 0
	global_load_dword v16, v2, s[0:1] nt
	s_add_u32 s0, s0, 0x4000
	s_addc_u32 s1, s1, 0
	global_load_dword v17, v2, s[0:1] nt
	s_add_u32 s0, s0, 0x4000
	s_addc_u32 s1, s1, 0
	global_load_dword v18, v2, s[0:1] nt
	s_add_u32 s0, s0, 0x4000
	s_addc_u32 s1, s1, 0
	global_load_dword v19, v2, s[0:1] nt
	s_add_u32 s0, s0, 0x4000
	s_addc_u32 s1, s1, 0
	global_load_dword v20, v2, s[0:1] nt
	s_add_u32 s0, s0, 0x4000
	s_addc_u32 s1, s1, 0
	global_load_dword v21, v2, s[0:1] nt
	s_add_u32 s0, s0, 0x4000
	s_addc_u32 s1, s1, 0
	global_load_dword v22, v2, s[0:1] nt
	s_add_u32 s0, s0, 0x4000
	s_addc_u32 s1, s1, 0
	global_load_dword v23, v2, s[0:1] nt
	s_add_u32 s0, s0, 0x4000
	s_addc_u32 s1, s1, 0
	global_load_dword v24, v2, s[0:1] nt
	s_add_u32 s0, s0, 0x4000
	s_addc_u32 s1, s1, 0
	global_load_dword v25, v2, s[0:1] nt
	s_add_u32 s0, s0, 0x4000
	s_addc_u32 s1, s1, 0
	global_load_dword v26, v2, s[0:1] nt
	s_add_u32 s0, s0, 0x4000
	s_addc_u32 s1, s1, 0
	global_load_dword v27, v2, s[0:1] nt
	s_add_u32 s0, s0, 0x4000
	s_addc_u32 s1, s1, 0
	global_load_dword v28, v2, s[0:1] nt
	s_add_u32 s0, s0, 0x4000
	s_addc_u32 s1, s1, 0
	global_load_dword v29, v2, s[0:1] nt
	s_add_u32 s0, s0, 0x4000
	s_addc_u32 s1, s1, 0
	global_load_dword v30, v2, s[0:1] nt
	s_add_u32 s0, s0, 0x4000
	s_addc_u32 s1, s1, 0
	global_load_dword v31, v2, s[0:1] nt
	s_add_u32 s0, s0, 0x4000
	s_addc_u32 s1, s1, 0
	global_load_dword v32, v2, s[0:1] nt
	s_add_u32 s0, s0, 0x4000
	s_addc_u32 s1, s1, 0
	global_load_dword v33, v2, s[0:1] nt
	s_add_u32 s0, s0, 0x4000
	s_addc_u32 s1, s1, 0
	global_load_dword v34, v2, s[0:1] nt
	s_add_u32 s0, s0, 0x4000
	s_addc_u32 s1, s1, 0
	global_load_dword v35, v2, s[0:1] nt
	s_add_u32 s0, s0, 0x4000
	s_addc_u32 s1, s1, 0
	global_load_dword v36, v2, s[0:1] nt
	s_add_u32 s0, s0, 0x4000
	s_addc_u32 s1, s1, 0
	global_load_dword v37, v2, s[0:1] nt
	s_add_u32 s0, s0, 0x4000
	s_addc_u32 s1, s1, 0
	global_load_dword v38, v2, s[0:1] nt
	s_add_u32 s0, s0, 0x4000
	s_addc_u32 s1, s1, 0
	global_load_dword v39, v2, s[0:1] nt
	s_add_u32 s0, s0, 0x4000
	s_addc_u32 s1, s1, 0
	global_load_dword v40, v2, s[0:1] nt
	s_add_u32 s0, s0, 0x4000
	s_addc_u32 s1, s1, 0
	global_load_dword v41, v2, s[0:1] nt
	s_add_u32 s0, s0, 0x4000
	s_addc_u32 s1, s1, 0
	global_load_dword v42, v2, s[0:1] nt
	s_add_u32 s0, s0, 0x4000
	s_addc_u32 s1, s1, 0
	global_load_dword v43, v2, s[0:1] nt
	s_waitcnt vmcnt(29)
	v_max3_f32 v1, |v12|, |v13|, |v14|
	s_waitcnt vmcnt(27)
	v_max3_f32 v1, v1, |v15|, |v16|
	s_waitcnt vmcnt(25)
	v_max3_f32 v1, v1, |v17|, |v18|
	s_waitcnt vmcnt(23)
	v_max3_f32 v1, v1, |v19|, |v20|
	s_waitcnt vmcnt(21)
	v_max3_f32 v1, v1, |v21|, |v22|
	s_waitcnt vmcnt(19)
	v_max3_f32 v1, v1, |v23|, |v24|
	s_waitcnt vmcnt(17)
	v_max3_f32 v1, v1, |v25|, |v26|
	s_waitcnt vmcnt(15)
	v_max3_f32 v1, v1, |v27|, |v28|
	s_waitcnt vmcnt(13)
	v_max3_f32 v1, v1, |v29|, |v30|
	s_waitcnt vmcnt(11)
	v_max3_f32 v1, v1, |v31|, |v32|
	s_waitcnt vmcnt(9)
	v_max3_f32 v1, v1, |v33|, |v34|
	s_waitcnt vmcnt(7)
	v_max3_f32 v1, v1, |v35|, |v36|
	s_waitcnt vmcnt(5)
	v_max3_f32 v1, v1, |v37|, |v38|
	s_waitcnt vmcnt(3)
	v_max3_f32 v1, v1, |v39|, |v40|
	s_waitcnt vmcnt(1)
	v_max3_f32 v1, v1, |v41|, |v42|
	s_waitcnt vmcnt(0)
	v_max_f32_e64 v1, v1, |v43|
	v_xor_b32_e32 v2, 32, v54
	v_lshlrev_b32_e32 v2, 2, v2
	ds_bpermute_b32 v2, v2, v1
	v_readlane_b32 s2, v252, 43
	v_readlane_b32 s3, v252, 44
	s_lshl_b32 s4, s33, 7
	s_sub_u32 s4, s4, 0xc0000
	s_add_u32 s2, s2, s4
	s_addc_u32 s3, s3, 0
	v_readlane_b32 s22, v252, 51
	v_readlane_b32 s23, v252, 52
	s_waitcnt lgkmcnt(0)
	v_max_f32_e32 v1, v1, v2
	v_lshlrev_b32_e32 v2, 2, v148
	s_and_saveexec_b64 s[4:5], s[22:23]
	global_store_dword v2, v1, s[2:3]
	s_or_b64 exec, exec, s[4:5]
